# grid barrier: member workgroups poll the top generation word directly (one hop fewer), per-XCD generation add dropped
# speedup vs baseline: 1.0166x; 1.0026x over previous
; __device__ __forceinline__ unsigned xb_add(unsigned* p, unsigned v) { return __hip_atomic_fetch_add(p, v, __ATOMIC_RELAXED, __HIP_MEMORY_SCOPE_AGENT); }
; __device__ __forceinline__ void xcd_barrier(const XcdBarrier& b) {
;     ...
;             __builtin_amdgcn_fence(__ATOMIC_ACQUIRE, "agent");
;             xb_add(&bar[XB_XGEN(b.x)], 1u);
;             asm volatile("s_waitcnt vmcnt(0)" ::: "memory");
.LBB0_190:
	s_or_b64 exec, exec, s[0:1]
	v_readlane_b32 s0, v247, 57
	v_readlane_b32 s1, v247, 58
	s_waitcnt vmcnt(0)
	buffer_inv sc1
	s_nop 2
	s_waitcnt vmcnt(0)

; __device__ __forceinline__ unsigned xb_ld(unsigned* p)              { return __hip_atomic_load(p, __ATOMIC_RELAXED, __HIP_MEMORY_SCOPE_AGENT); }
; __device__ __forceinline__ unsigned xb_add(unsigned* p, unsigned v) { return __hip_atomic_fetch_add(p, v, __ATOMIC_RELAXED, __HIP_MEMORY_SCOPE_AGENT); }
; #define XB_SPIN(cond, bar) do { unsigned _sp = 0; while (cond) { __builtin_amdgcn_s_sleep(1); \
;     if ((++_sp & 255u) == 0u) { if (xb_ld(&(bar)[XB_TMO])) break; if (_sp > XB_SPIN_CAP) { atomicAdd(&(bar)[XB_TMO], 1u); break; } } } } while (0)
; __device__ __forceinline__ void xcd_barrier(const XcdBarrier& b) {
;     ...
;         const unsigned old = xb_add(&bar[XB_XSUB(b.x)], 1u);
;         const unsigned gen = old / nloc;
;         if (old + 1u == (gen + 1u) * nloc) {
;             __builtin_amdgcn_fence(__ATOMIC_RELEASE, "agent");
;             asm volatile("s_waitcnt vmcnt(0)" ::: "memory");
;             const unsigned og = xb_add(&bar[XB_TOP], 1u);
;             const unsigned tg = og / nx;
;             if (og + 1u == (tg + 1u) * nx) xb_add(&bar[XB_TOPGEN], 1u);
;             else XB_SPIN(xb_ld(&bar[XB_TOPGEN]) == tg, bar);
;             __builtin_amdgcn_fence(__ATOMIC_ACQUIRE, "agent");
;             xb_add(&bar[XB_XGEN(b.x)], 1u);
;             asm volatile("s_waitcnt vmcnt(0)" ::: "memory");
;         } else {
;             XB_SPIN(xb_ld(&bar[XB_XGEN(b.x)]) == gen, bar);
.LBB0_229:
	v_readlane_b32 s0, v247, 55
	v_readlane_b32 s1, v247, 56
	v_cvt_f32_u32_e32 v1, v2
	v_sub_u32_e32 v4, 0, v2
	v_rcp_iflag_f32_e32 v1, v1
	s_nop 1
	global_atomic_add v3, v153, v197, s[0:1] sc0
	v_mul_f32_e32 v1, 0x4f7ffffe, v1
	v_cvt_u32_f32_e32 v1, v1
	v_mul_lo_u32 v4, v4, v1
	v_mul_hi_u32 v4, v1, v4
	v_add_u32_e32 v1, v1, v4
	s_waitcnt vmcnt(0)
	v_mul_hi_u32 v1, v3, v1
	v_mul_lo_u32 v4, v1, v2
	v_sub_u32_e32 v4, v3, v4
	v_add_u32_e32 v5, 1, v1
	v_cmp_ge_u32_e32 vcc, v4, v2
	v_add_u32_e32 v3, 1, v3
	s_nop 0
	v_cndmask_b32_e32 v1, v1, v5, vcc
	v_sub_u32_e32 v5, v4, v2
	v_cndmask_b32_e32 v4, v4, v5, vcc
	v_add_u32_e32 v5, 1, v1
	v_cmp_ge_u32_e32 vcc, v4, v2
	s_nop 1
	v_cndmask_b32_e32 v1, v1, v5, vcc
	v_mul_lo_u32 v4, v2, v1
	v_add_u32_e32 v2, v4, v2
	v_cmp_ne_u32_e32 vcc, v3, v2
	s_and_saveexec_b64 s[0:1], vcc
	s_xor_b64 s[0:1], exec, s[0:1]
	s_cbranch_execz .LBB0_243
	v_readlane_b32 s2, v247, 61
	v_readlane_b32 s3, v247, 62
	s_waitcnt lgkmcnt(0)
	s_nop 3
	global_load_dword v0, v153, s[2:3] sc1
	s_waitcnt vmcnt(0)
	v_cmp_eq_u32_e32 vcc, v0, v1
	s_and_saveexec_b64 s[10:11], vcc
	s_cbranch_execz .LBB0_242
	s_mov_b32 s31, 1
	s_mov_b64 s[12:13], 0
	s_branch .LBB0_233

; __device__ __forceinline__ unsigned xb_ld(unsigned* p)              { return __hip_atomic_load(p, __ATOMIC_RELAXED, __HIP_MEMORY_SCOPE_AGENT); }
; __device__ __forceinline__ unsigned xb_add(unsigned* p, unsigned v) { return __hip_atomic_fetch_add(p, v, __ATOMIC_RELAXED, __HIP_MEMORY_SCOPE_AGENT); }
; #define XB_SPIN(cond, bar) do { unsigned _sp = 0; while (cond) { __builtin_amdgcn_s_sleep(1); \
;     if ((++_sp & 255u) == 0u) { if (xb_ld(&(bar)[XB_TMO])) break; if (_sp > XB_SPIN_CAP) { atomicAdd(&(bar)[XB_TMO], 1u); break; } } } } while (0)
; __device__ __forceinline__ void xcd_barrier(const XcdBarrier& b) {
;     ...
;             else XB_SPIN(xb_ld(&bar[XB_TOPGEN]) == tg, bar);
;             __builtin_amdgcn_fence(__ATOMIC_ACQUIRE, "agent");
;             xb_add(&bar[XB_XGEN(b.x)], 1u);
;             asm volatile("s_waitcnt vmcnt(0)" ::: "memory");
;         } else {
;             XB_SPIN(xb_ld(&bar[XB_XGEN(b.x)]) == gen, bar);
.LBB0_235:
	v_readlane_b32 s2, v247, 61
	v_readlane_b32 s3, v247, 62
	s_add_i32 s31, s31, 1
	s_mov_b64 s[18:19], -1
	s_nop 2
	global_load_dword v0, v153, s[2:3] sc1
	s_waitcnt vmcnt(0)
	v_cmp_ne_u32_e32 vcc, v0, v1
	s_orn2_b64 s[16:17], vcc, exec
	s_branch .LBB0_232

; __device__ __forceinline__ unsigned xb_ld(unsigned* p)              { return __hip_atomic_load(p, __ATOMIC_RELAXED, __HIP_MEMORY_SCOPE_AGENT); }
; __device__ __forceinline__ unsigned xb_add(unsigned* p, unsigned v) { return __hip_atomic_fetch_add(p, v, __ATOMIC_RELAXED, __HIP_MEMORY_SCOPE_AGENT); }
; #define XB_SPIN(cond, bar) do { unsigned _sp = 0; while (cond) { __builtin_amdgcn_s_sleep(1); \
;     if ((++_sp & 255u) == 0u) { if (xb_ld(&(bar)[XB_TMO])) break; if (_sp > XB_SPIN_CAP) { atomicAdd(&(bar)[XB_TMO], 1u); break; } } } } while (0)
; __device__ __forceinline__ void xcd_barrier(const XcdBarrier& b) {
;     ...
;         const unsigned old = xb_add(&bar[XB_XSUB(b.x)], 1u);
;         const unsigned gen = old / nloc;
;         if (old + 1u == (gen + 1u) * nloc) {
;             __builtin_amdgcn_fence(__ATOMIC_RELEASE, "agent");
;             asm volatile("s_waitcnt vmcnt(0)" ::: "memory");
;             const unsigned og = xb_add(&bar[XB_TOP], 1u);
;             const unsigned tg = og / nx;
;             if (og + 1u == (tg + 1u) * nx) xb_add(&bar[XB_TOPGEN], 1u);
;             else XB_SPIN(xb_ld(&bar[XB_TOPGEN]) == tg, bar);
;             __builtin_amdgcn_fence(__ATOMIC_ACQUIRE, "agent");
;             xb_add(&bar[XB_XGEN(b.x)], 1u);
;             asm volatile("s_waitcnt vmcnt(0)" ::: "memory");
;         } else {
;             XB_SPIN(xb_ld(&bar[XB_XGEN(b.x)]) == gen, bar);
.LBB0_382:
	v_readlane_b32 s0, v247, 55
	v_readlane_b32 s1, v247, 56
	v_cvt_f32_u32_e32 v1, v2
	v_sub_u32_e32 v4, 0, v2
	v_rcp_iflag_f32_e32 v1, v1
	s_nop 1
	global_atomic_add v3, v153, v197, s[0:1] sc0
	v_mul_f32_e32 v1, 0x4f7ffffe, v1
	v_cvt_u32_f32_e32 v1, v1
	v_mul_lo_u32 v4, v4, v1
	v_mul_hi_u32 v4, v1, v4
	v_add_u32_e32 v1, v1, v4
	s_waitcnt vmcnt(0)
	v_mul_hi_u32 v1, v3, v1
	v_mul_lo_u32 v4, v1, v2
	v_sub_u32_e32 v4, v3, v4
	v_add_u32_e32 v5, 1, v1
	v_cmp_ge_u32_e32 vcc, v4, v2
	v_add_u32_e32 v3, 1, v3
	s_nop 0
	v_cndmask_b32_e32 v1, v1, v5, vcc
	v_sub_u32_e32 v5, v4, v2
	v_cndmask_b32_e32 v4, v4, v5, vcc
	v_add_u32_e32 v5, 1, v1
	v_cmp_ge_u32_e32 vcc, v4, v2
	s_nop 1
	v_cndmask_b32_e32 v1, v1, v5, vcc
	v_mul_lo_u32 v4, v2, v1
	v_add_u32_e32 v2, v4, v2
	v_cmp_ne_u32_e32 vcc, v3, v2
	s_and_saveexec_b64 s[0:1], vcc
	s_xor_b64 s[0:1], exec, s[0:1]
	s_cbranch_execz .LBB0_396
	v_readlane_b32 s2, v247, 61
	v_readlane_b32 s3, v247, 62
	s_waitcnt lgkmcnt(0)
	s_nop 3
	global_load_dword v0, v153, s[2:3] sc1
	s_waitcnt vmcnt(0)
	v_cmp_eq_u32_e32 vcc, v0, v1
	s_and_saveexec_b64 s[10:11], vcc
	s_cbranch_execz .LBB0_395
	s_mov_b32 s40, 1
	s_mov_b64 s[12:13], 0
	s_branch .LBB0_386

; __device__ __forceinline__ unsigned xb_ld(unsigned* p)              { return __hip_atomic_load(p, __ATOMIC_RELAXED, __HIP_MEMORY_SCOPE_AGENT); }
; __device__ __forceinline__ unsigned xb_add(unsigned* p, unsigned v) { return __hip_atomic_fetch_add(p, v, __ATOMIC_RELAXED, __HIP_MEMORY_SCOPE_AGENT); }
; #define XB_SPIN(cond, bar) do { unsigned _sp = 0; while (cond) { __builtin_amdgcn_s_sleep(1); \
;     if ((++_sp & 255u) == 0u) { if (xb_ld(&(bar)[XB_TMO])) break; if (_sp > XB_SPIN_CAP) { atomicAdd(&(bar)[XB_TMO], 1u); break; } } } } while (0)
; __device__ __forceinline__ void xcd_barrier(const XcdBarrier& b) {
;     ...
;             else XB_SPIN(xb_ld(&bar[XB_TOPGEN]) == tg, bar);
;             __builtin_amdgcn_fence(__ATOMIC_ACQUIRE, "agent");
;             xb_add(&bar[XB_XGEN(b.x)], 1u);
;             asm volatile("s_waitcnt vmcnt(0)" ::: "memory");
;         } else {
;             XB_SPIN(xb_ld(&bar[XB_XGEN(b.x)]) == gen, bar);
.LBB0_388:
	v_readlane_b32 s2, v247, 61
	v_readlane_b32 s3, v247, 62
	s_add_i32 s40, s40, 1
	s_mov_b64 s[18:19], -1
	s_nop 2
	global_load_dword v0, v153, s[2:3] sc1
	s_waitcnt vmcnt(0)
	v_cmp_ne_u32_e32 vcc, v0, v1
	s_orn2_b64 s[16:17], vcc, exec
	s_branch .LBB0_385

; __device__ __forceinline__ unsigned xb_ld(unsigned* p)              { return __hip_atomic_load(p, __ATOMIC_RELAXED, __HIP_MEMORY_SCOPE_AGENT); }
; __device__ __forceinline__ unsigned xb_add(unsigned* p, unsigned v) { return __hip_atomic_fetch_add(p, v, __ATOMIC_RELAXED, __HIP_MEMORY_SCOPE_AGENT); }
; #define XB_SPIN(cond, bar) do { unsigned _sp = 0; while (cond) { __builtin_amdgcn_s_sleep(1); \
;     if ((++_sp & 255u) == 0u) { if (xb_ld(&(bar)[XB_TMO])) break; if (_sp > XB_SPIN_CAP) { atomicAdd(&(bar)[XB_TMO], 1u); break; } } } } while (0)
; __device__ __forceinline__ void xcd_barrier(const XcdBarrier& b) {
;     ...
;         const unsigned old = xb_add(&bar[XB_XSUB(b.x)], 1u);
;         const unsigned gen = old / nloc;
;         if (old + 1u == (gen + 1u) * nloc) {
;             __builtin_amdgcn_fence(__ATOMIC_RELEASE, "agent");
;             asm volatile("s_waitcnt vmcnt(0)" ::: "memory");
;             const unsigned og = xb_add(&bar[XB_TOP], 1u);
;             const unsigned tg = og / nx;
;             if (og + 1u == (tg + 1u) * nx) xb_add(&bar[XB_TOPGEN], 1u);
;             else XB_SPIN(xb_ld(&bar[XB_TOPGEN]) == tg, bar);
;             __builtin_amdgcn_fence(__ATOMIC_ACQUIRE, "agent");
;             xb_add(&bar[XB_XGEN(b.x)], 1u);
;             asm volatile("s_waitcnt vmcnt(0)" ::: "memory");
;         } else {
;             XB_SPIN(xb_ld(&bar[XB_XGEN(b.x)]) == gen, bar);
.LBB0_790:
	v_readlane_b32 s0, v247, 55
	v_readlane_b32 s1, v247, 56
	v_cvt_f32_u32_e32 v1, v2
	v_sub_u32_e32 v4, 0, v2
	v_rcp_iflag_f32_e32 v1, v1
	s_nop 1
	global_atomic_add v3, v153, v197, s[0:1] sc0
	v_mul_f32_e32 v1, 0x4f7ffffe, v1
	v_cvt_u32_f32_e32 v1, v1
	v_mul_lo_u32 v4, v4, v1
	v_mul_hi_u32 v4, v1, v4
	v_add_u32_e32 v1, v1, v4
	s_waitcnt vmcnt(0)
	v_mul_hi_u32 v1, v3, v1
	v_mul_lo_u32 v4, v1, v2
	v_sub_u32_e32 v4, v3, v4
	v_add_u32_e32 v5, 1, v1
	v_cmp_ge_u32_e32 vcc, v4, v2
	v_add_u32_e32 v3, 1, v3
	s_nop 0
	v_cndmask_b32_e32 v1, v1, v5, vcc
	v_sub_u32_e32 v5, v4, v2
	v_cndmask_b32_e32 v4, v4, v5, vcc
	v_add_u32_e32 v5, 1, v1
	v_cmp_ge_u32_e32 vcc, v4, v2
	s_nop 1
	v_cndmask_b32_e32 v1, v1, v5, vcc
	v_mul_lo_u32 v4, v2, v1
	v_add_u32_e32 v2, v4, v2
	v_cmp_ne_u32_e32 vcc, v3, v2
	s_and_saveexec_b64 s[0:1], vcc
	s_xor_b64 s[0:1], exec, s[0:1]
	s_cbranch_execz .LBB0_804
	v_readlane_b32 s2, v247, 61
	v_readlane_b32 s3, v247, 62
	s_waitcnt lgkmcnt(0)
	s_nop 3
	global_load_dword v0, v153, s[2:3] sc1
	s_waitcnt vmcnt(0)
	v_cmp_eq_u32_e32 vcc, v0, v1
	s_and_saveexec_b64 s[10:11], vcc
	s_cbranch_execz .LBB0_803
	s_mov_b32 s5, 1
	s_mov_b64 s[12:13], 0
	s_branch .LBB0_794

; __device__ __forceinline__ unsigned xb_ld(unsigned* p)              { return __hip_atomic_load(p, __ATOMIC_RELAXED, __HIP_MEMORY_SCOPE_AGENT); }
; __device__ __forceinline__ unsigned xb_add(unsigned* p, unsigned v) { return __hip_atomic_fetch_add(p, v, __ATOMIC_RELAXED, __HIP_MEMORY_SCOPE_AGENT); }
; #define XB_SPIN(cond, bar) do { unsigned _sp = 0; while (cond) { __builtin_amdgcn_s_sleep(1); \
;     if ((++_sp & 255u) == 0u) { if (xb_ld(&(bar)[XB_TMO])) break; if (_sp > XB_SPIN_CAP) { atomicAdd(&(bar)[XB_TMO], 1u); break; } } } } while (0)
; __device__ __forceinline__ void xcd_barrier(const XcdBarrier& b) {
;     ...
;             else XB_SPIN(xb_ld(&bar[XB_TOPGEN]) == tg, bar);
;             __builtin_amdgcn_fence(__ATOMIC_ACQUIRE, "agent");
;             xb_add(&bar[XB_XGEN(b.x)], 1u);
;             asm volatile("s_waitcnt vmcnt(0)" ::: "memory");
;         } else {
;             XB_SPIN(xb_ld(&bar[XB_XGEN(b.x)]) == gen, bar);
.LBB0_796:
	v_readlane_b32 s2, v247, 61
	v_readlane_b32 s3, v247, 62
	s_add_i32 s5, s5, 1
	s_mov_b64 s[18:19], -1
	s_nop 2
	global_load_dword v0, v153, s[2:3] sc1
	s_waitcnt vmcnt(0)
	v_cmp_ne_u32_e32 vcc, v0, v1
	s_orn2_b64 s[16:17], vcc, exec
	s_branch .LBB0_793

; __device__ __forceinline__ unsigned xb_ld(unsigned* p)              { return __hip_atomic_load(p, __ATOMIC_RELAXED, __HIP_MEMORY_SCOPE_AGENT); }
; __device__ __forceinline__ unsigned xb_add(unsigned* p, unsigned v) { return __hip_atomic_fetch_add(p, v, __ATOMIC_RELAXED, __HIP_MEMORY_SCOPE_AGENT); }
; #define XB_SPIN(cond, bar) do { unsigned _sp = 0; while (cond) { __builtin_amdgcn_s_sleep(1); \
;     if ((++_sp & 255u) == 0u) { if (xb_ld(&(bar)[XB_TMO])) break; if (_sp > XB_SPIN_CAP) { atomicAdd(&(bar)[XB_TMO], 1u); break; } } } } while (0)
; __device__ __forceinline__ void xcd_barrier(const XcdBarrier& b) {
;     ...
;         const unsigned old = xb_add(&bar[XB_XSUB(b.x)], 1u);
;         const unsigned gen = old / nloc;
;         if (old + 1u == (gen + 1u) * nloc) {
;             __builtin_amdgcn_fence(__ATOMIC_RELEASE, "agent");
;             asm volatile("s_waitcnt vmcnt(0)" ::: "memory");
;             const unsigned og = xb_add(&bar[XB_TOP], 1u);
;             const unsigned tg = og / nx;
;             if (og + 1u == (tg + 1u) * nx) xb_add(&bar[XB_TOPGEN], 1u);
;             else XB_SPIN(xb_ld(&bar[XB_TOPGEN]) == tg, bar);
;             __builtin_amdgcn_fence(__ATOMIC_ACQUIRE, "agent");
;             xb_add(&bar[XB_XGEN(b.x)], 1u);
;             asm volatile("s_waitcnt vmcnt(0)" ::: "memory");
;         } else {
;             XB_SPIN(xb_ld(&bar[XB_XGEN(b.x)]) == gen, bar);
.LBB0_1110:
	v_readlane_b32 s0, v247, 55
	v_readlane_b32 s1, v247, 56
	v_cvt_f32_u32_e32 v1, v2
	v_sub_u32_e32 v4, 0, v2
	v_rcp_iflag_f32_e32 v1, v1
	s_nop 1
	global_atomic_add v3, v153, v197, s[0:1] sc0
	v_mul_f32_e32 v1, 0x4f7ffffe, v1
	v_cvt_u32_f32_e32 v1, v1
	v_mul_lo_u32 v4, v4, v1
	v_mul_hi_u32 v4, v1, v4
	v_add_u32_e32 v1, v1, v4
	s_waitcnt vmcnt(0)
	v_mul_hi_u32 v1, v3, v1
	v_mul_lo_u32 v4, v1, v2
	v_sub_u32_e32 v4, v3, v4
	v_add_u32_e32 v5, 1, v1
	v_cmp_ge_u32_e32 vcc, v4, v2
	v_add_u32_e32 v3, 1, v3
	s_nop 0
	v_cndmask_b32_e32 v1, v1, v5, vcc
	v_sub_u32_e32 v5, v4, v2
	v_cndmask_b32_e32 v4, v4, v5, vcc
	v_add_u32_e32 v5, 1, v1
	v_cmp_ge_u32_e32 vcc, v4, v2
	s_nop 1
	v_cndmask_b32_e32 v1, v1, v5, vcc
	v_mul_lo_u32 v4, v2, v1
	v_add_u32_e32 v2, v4, v2
	v_cmp_ne_u32_e32 vcc, v3, v2
	s_and_saveexec_b64 s[0:1], vcc
	s_xor_b64 s[0:1], exec, s[0:1]
	s_cbranch_execz .LBB0_1124
	v_readlane_b32 s2, v247, 61
	v_readlane_b32 s3, v247, 62
	s_waitcnt lgkmcnt(0)
	s_nop 3
	global_load_dword v0, v153, s[2:3] sc1
	s_waitcnt vmcnt(0)
	v_cmp_eq_u32_e32 vcc, v0, v1
	s_and_saveexec_b64 s[8:9], vcc
	s_cbranch_execz .LBB0_1123
	s_mov_b32 s41, 1
	s_mov_b64 s[10:11], 0
	s_branch .LBB0_1114

; __device__ __forceinline__ unsigned xb_ld(unsigned* p)              { return __hip_atomic_load(p, __ATOMIC_RELAXED, __HIP_MEMORY_SCOPE_AGENT); }
; __device__ __forceinline__ unsigned xb_add(unsigned* p, unsigned v) { return __hip_atomic_fetch_add(p, v, __ATOMIC_RELAXED, __HIP_MEMORY_SCOPE_AGENT); }
; #define XB_SPIN(cond, bar) do { unsigned _sp = 0; while (cond) { __builtin_amdgcn_s_sleep(1); \
;     if ((++_sp & 255u) == 0u) { if (xb_ld(&(bar)[XB_TMO])) break; if (_sp > XB_SPIN_CAP) { atomicAdd(&(bar)[XB_TMO], 1u); break; } } } } while (0)
; __device__ __forceinline__ void xcd_barrier(const XcdBarrier& b) {
;     ...
;             else XB_SPIN(xb_ld(&bar[XB_TOPGEN]) == tg, bar);
;             __builtin_amdgcn_fence(__ATOMIC_ACQUIRE, "agent");
;             xb_add(&bar[XB_XGEN(b.x)], 1u);
;             asm volatile("s_waitcnt vmcnt(0)" ::: "memory");
;         } else {
;             XB_SPIN(xb_ld(&bar[XB_XGEN(b.x)]) == gen, bar);
.LBB0_1116:
	v_readlane_b32 s2, v247, 61
	v_readlane_b32 s3, v247, 62
	s_add_i32 s41, s41, 1
	s_mov_b64 s[16:17], -1
	s_nop 2
	global_load_dword v0, v153, s[2:3] sc1
	s_waitcnt vmcnt(0)
	v_cmp_ne_u32_e32 vcc, v0, v1
	s_orn2_b64 s[14:15], vcc, exec
	s_branch .LBB0_1113

; __device__ __forceinline__ unsigned xb_ld(unsigned* p)              { return __hip_atomic_load(p, __ATOMIC_RELAXED, __HIP_MEMORY_SCOPE_AGENT); }
; __device__ __forceinline__ unsigned xb_add(unsigned* p, unsigned v) { return __hip_atomic_fetch_add(p, v, __ATOMIC_RELAXED, __HIP_MEMORY_SCOPE_AGENT); }
; #define XB_SPIN(cond, bar) do { unsigned _sp = 0; while (cond) { __builtin_amdgcn_s_sleep(1); \
;     if ((++_sp & 255u) == 0u) { if (xb_ld(&(bar)[XB_TMO])) break; if (_sp > XB_SPIN_CAP) { atomicAdd(&(bar)[XB_TMO], 1u); break; } } } } while (0)
; __device__ __forceinline__ void xcd_barrier(const XcdBarrier& b) {
;     ...
;         const unsigned old = xb_add(&bar[XB_XSUB(b.x)], 1u);
;         const unsigned gen = old / nloc;
;         if (old + 1u == (gen + 1u) * nloc) {
;             __builtin_amdgcn_fence(__ATOMIC_RELEASE, "agent");
;             asm volatile("s_waitcnt vmcnt(0)" ::: "memory");
;             const unsigned og = xb_add(&bar[XB_TOP], 1u);
;             const unsigned tg = og / nx;
;             if (og + 1u == (tg + 1u) * nx) xb_add(&bar[XB_TOPGEN], 1u);
;             else XB_SPIN(xb_ld(&bar[XB_TOPGEN]) == tg, bar);
;             __builtin_amdgcn_fence(__ATOMIC_ACQUIRE, "agent");
;             xb_add(&bar[XB_XGEN(b.x)], 1u);
;             asm volatile("s_waitcnt vmcnt(0)" ::: "memory");
;         } else {
;             XB_SPIN(xb_ld(&bar[XB_XGEN(b.x)]) == gen, bar);
.LBB0_1328:
	v_readlane_b32 s0, v247, 55
	v_readlane_b32 s1, v247, 56
	v_cvt_f32_u32_e32 v1, v2
	v_sub_u32_e32 v4, 0, v2
	v_rcp_iflag_f32_e32 v1, v1
	s_nop 1
	global_atomic_add v3, v153, v197, s[0:1] sc0
	v_mul_f32_e32 v1, 0x4f7ffffe, v1
	v_cvt_u32_f32_e32 v1, v1
	v_mul_lo_u32 v4, v4, v1
	v_mul_hi_u32 v4, v1, v4
	v_add_u32_e32 v1, v1, v4
	s_waitcnt vmcnt(0)
	v_mul_hi_u32 v1, v3, v1
	v_mul_lo_u32 v4, v1, v2
	v_sub_u32_e32 v4, v3, v4
	v_add_u32_e32 v5, 1, v1
	v_cmp_ge_u32_e32 vcc, v4, v2
	v_add_u32_e32 v3, 1, v3
	s_nop 0
	v_cndmask_b32_e32 v1, v1, v5, vcc
	v_sub_u32_e32 v5, v4, v2
	v_cndmask_b32_e32 v4, v4, v5, vcc
	v_add_u32_e32 v5, 1, v1
	v_cmp_ge_u32_e32 vcc, v4, v2
	s_nop 1
	v_cndmask_b32_e32 v1, v1, v5, vcc
	v_mul_lo_u32 v4, v2, v1
	v_add_u32_e32 v2, v4, v2
	v_cmp_ne_u32_e32 vcc, v3, v2
	s_and_saveexec_b64 s[0:1], vcc
	s_xor_b64 s[0:1], exec, s[0:1]
	s_cbranch_execz .LBB0_1342
	v_readlane_b32 s2, v247, 61
	v_readlane_b32 s3, v247, 62
	s_waitcnt lgkmcnt(0)
	s_nop 3
	global_load_dword v0, v153, s[2:3] sc1
	s_waitcnt vmcnt(0)
	v_cmp_eq_u32_e32 vcc, v0, v1
	s_and_saveexec_b64 s[10:11], vcc
	s_cbranch_execz .LBB0_1341
	s_mov_b32 s43, 1
	s_mov_b64 s[12:13], 0
	s_branch .LBB0_1332

; __device__ __forceinline__ unsigned xb_ld(unsigned* p)              { return __hip_atomic_load(p, __ATOMIC_RELAXED, __HIP_MEMORY_SCOPE_AGENT); }
; __device__ __forceinline__ unsigned xb_add(unsigned* p, unsigned v) { return __hip_atomic_fetch_add(p, v, __ATOMIC_RELAXED, __HIP_MEMORY_SCOPE_AGENT); }
; #define XB_SPIN(cond, bar) do { unsigned _sp = 0; while (cond) { __builtin_amdgcn_s_sleep(1); \
;     if ((++_sp & 255u) == 0u) { if (xb_ld(&(bar)[XB_TMO])) break; if (_sp > XB_SPIN_CAP) { atomicAdd(&(bar)[XB_TMO], 1u); break; } } } } while (0)
; __device__ __forceinline__ void xcd_barrier(const XcdBarrier& b) {
;     ...
;             else XB_SPIN(xb_ld(&bar[XB_TOPGEN]) == tg, bar);
;             __builtin_amdgcn_fence(__ATOMIC_ACQUIRE, "agent");
;             xb_add(&bar[XB_XGEN(b.x)], 1u);
;             asm volatile("s_waitcnt vmcnt(0)" ::: "memory");
;         } else {
;             XB_SPIN(xb_ld(&bar[XB_XGEN(b.x)]) == gen, bar);
.LBB0_1334:
	v_readlane_b32 s2, v247, 61
	v_readlane_b32 s3, v247, 62
	s_add_i32 s43, s43, 1
	s_mov_b64 s[18:19], -1
	s_nop 2
	global_load_dword v0, v153, s[2:3] sc1
	s_waitcnt vmcnt(0)
	v_cmp_ne_u32_e32 vcc, v0, v1
	s_orn2_b64 s[16:17], vcc, exec
	s_branch .LBB0_1331

; __device__ __forceinline__ unsigned xb_ld(unsigned* p)              { return __hip_atomic_load(p, __ATOMIC_RELAXED, __HIP_MEMORY_SCOPE_AGENT); }
; __device__ __forceinline__ unsigned xb_add(unsigned* p, unsigned v) { return __hip_atomic_fetch_add(p, v, __ATOMIC_RELAXED, __HIP_MEMORY_SCOPE_AGENT); }
; #define XB_SPIN(cond, bar) do { unsigned _sp = 0; while (cond) { __builtin_amdgcn_s_sleep(1); \
;     if ((++_sp & 255u) == 0u) { if (xb_ld(&(bar)[XB_TMO])) break; if (_sp > XB_SPIN_CAP) { atomicAdd(&(bar)[XB_TMO], 1u); break; } } } } while (0)
; __device__ __forceinline__ void xcd_barrier(const XcdBarrier& b) {
;     ...
;         const unsigned old = xb_add(&bar[XB_XSUB(b.x)], 1u);
;         const unsigned gen = old / nloc;
;         if (old + 1u == (gen + 1u) * nloc) {
;             __builtin_amdgcn_fence(__ATOMIC_RELEASE, "agent");
;             asm volatile("s_waitcnt vmcnt(0)" ::: "memory");
;             const unsigned og = xb_add(&bar[XB_TOP], 1u);
;             const unsigned tg = og / nx;
;             if (og + 1u == (tg + 1u) * nx) xb_add(&bar[XB_TOPGEN], 1u);
;             else XB_SPIN(xb_ld(&bar[XB_TOPGEN]) == tg, bar);
;             __builtin_amdgcn_fence(__ATOMIC_ACQUIRE, "agent");
;             xb_add(&bar[XB_XGEN(b.x)], 1u);
;             asm volatile("s_waitcnt vmcnt(0)" ::: "memory");
;         } else {
;             XB_SPIN(xb_ld(&bar[XB_XGEN(b.x)]) == gen, bar);
.LBB0_1707:
	v_readlane_b32 s0, v247, 55
	v_readlane_b32 s1, v247, 56
	v_cvt_f32_u32_e32 v1, v2
	v_sub_u32_e32 v4, 0, v2
	v_rcp_iflag_f32_e32 v1, v1
	s_nop 1
	global_atomic_add v3, v153, v197, s[0:1] sc0
	v_mul_f32_e32 v1, 0x4f7ffffe, v1
	v_cvt_u32_f32_e32 v1, v1
	v_mul_lo_u32 v4, v4, v1
	v_mul_hi_u32 v4, v1, v4
	v_add_u32_e32 v1, v1, v4
	s_waitcnt vmcnt(0)
	v_mul_hi_u32 v1, v3, v1
	v_mul_lo_u32 v4, v1, v2
	v_sub_u32_e32 v4, v3, v4
	v_add_u32_e32 v5, 1, v1
	v_cmp_ge_u32_e32 vcc, v4, v2
	v_add_u32_e32 v3, 1, v3
	s_nop 0
	v_cndmask_b32_e32 v1, v1, v5, vcc
	v_sub_u32_e32 v5, v4, v2
	v_cndmask_b32_e32 v4, v4, v5, vcc
	v_add_u32_e32 v5, 1, v1
	v_cmp_ge_u32_e32 vcc, v4, v2
	s_nop 1
	v_cndmask_b32_e32 v1, v1, v5, vcc
	v_mul_lo_u32 v4, v2, v1
	v_add_u32_e32 v2, v4, v2
	v_cmp_ne_u32_e32 vcc, v3, v2
	s_and_saveexec_b64 s[0:1], vcc
	s_xor_b64 s[0:1], exec, s[0:1]
	s_cbranch_execz .LBB0_1721
	v_readlane_b32 s2, v247, 61
	v_readlane_b32 s3, v247, 62
	s_waitcnt lgkmcnt(0)
	s_nop 3
	global_load_dword v0, v153, s[2:3] sc1
	s_waitcnt vmcnt(0)
	v_cmp_eq_u32_e32 vcc, v0, v1
	s_and_saveexec_b64 s[8:9], vcc
	s_cbranch_execz .LBB0_1720
	s_mov_b32 s5, 1
	s_mov_b64 s[10:11], 0
	s_branch .LBB0_1711

; __device__ __forceinline__ unsigned xb_ld(unsigned* p)              { return __hip_atomic_load(p, __ATOMIC_RELAXED, __HIP_MEMORY_SCOPE_AGENT); }
; __device__ __forceinline__ unsigned xb_add(unsigned* p, unsigned v) { return __hip_atomic_fetch_add(p, v, __ATOMIC_RELAXED, __HIP_MEMORY_SCOPE_AGENT); }
; #define XB_SPIN(cond, bar) do { unsigned _sp = 0; while (cond) { __builtin_amdgcn_s_sleep(1); \
;     if ((++_sp & 255u) == 0u) { if (xb_ld(&(bar)[XB_TMO])) break; if (_sp > XB_SPIN_CAP) { atomicAdd(&(bar)[XB_TMO], 1u); break; } } } } while (0)
; __device__ __forceinline__ void xcd_barrier(const XcdBarrier& b) {
;     ...
;             else XB_SPIN(xb_ld(&bar[XB_TOPGEN]) == tg, bar);
;             __builtin_amdgcn_fence(__ATOMIC_ACQUIRE, "agent");
;             xb_add(&bar[XB_XGEN(b.x)], 1u);
;             asm volatile("s_waitcnt vmcnt(0)" ::: "memory");
;         } else {
;             XB_SPIN(xb_ld(&bar[XB_XGEN(b.x)]) == gen, bar);
.LBB0_1713:
	v_readlane_b32 s2, v247, 61
	v_readlane_b32 s3, v247, 62
	s_add_i32 s5, s5, 1
	s_mov_b64 s[16:17], -1
	s_nop 2
	global_load_dword v0, v153, s[2:3] sc1
	s_waitcnt vmcnt(0)
	v_cmp_ne_u32_e32 vcc, v0, v1
	s_orn2_b64 s[14:15], vcc, exec
	s_branch .LBB0_1710
